# baseline (speedup 1.0000x reference)
.LBB3_11:
	v_add_u32_e32 v172, s43, v207
	v_pk_fma_f32 v[244:245], v[244:245], -0.5, -0.5 op_sel_hi:[1,0,0]
	s_lshl_b32 s58, s42, 7
	v_pk_fma_f32 v[246:247], v[246:247], -0.5, -0.5 op_sel_hi:[1,0,0]
	s_add_i32 s59, s41, 0x400
	v_pk_fma_f32 v[248:249], v[248:249], -0.5, -0.5 op_sel_hi:[1,0,0]
	s_lshr_b32 s59, s59, 6
	v_pk_fma_f32 v[250:251], v[250:251], -0.5, -0.5 op_sel_hi:[1,0,0]
	s_bfe_u32 s60, s20, 0x1000c
	v_pk_fma_f32 v[252:253], v[252:253], -0.5, -0.5 op_sel_hi:[1,0,0]
	s_add_i32 s59, s59, s60
	v_pk_fma_f32 v[254:255], v[254:255], -0.5, -0.5 op_sel_hi:[1,0,0]
	s_lshl_b32 s59, s59, 19
	v_pk_fma_f32 v[232:233], v[232:233], -0.5, -0.5 op_sel_hi:[1,0,0]
	s_add_u32 s58, s58, s59
	v_pk_fma_f32 v[234:235], v[234:235], -0.5, -0.5 op_sel_hi:[1,0,0]
	s_add_u32 s58, s56, s58
	v_pk_mul_f32 v[134:135], v[244:245], v[246:247]
	s_addc_u32 s59, s57, 0
	v_pk_mul_f32 v[146:147], v[248:249], v[250:251]
	s_add_u32 s60, s58, 0x4000
	v_pk_mul_f32 v[180:181], v[252:253], v[254:255]
	s_addc_u32 s61, s59, 0
	v_pk_mul_f32 v[236:237], v[232:233], v[234:235]
	s_add_u32 s62, s58, 0x100000
	v_mul_f32_e32 v188, v134, v135
	s_addc_u32 s63, s59, 0
	v_mul_f32_e32 v190, v146, v147
	s_add_u32 s64, s62, 0x4000
	v_mul_f32_e32 v189, v180, v181
	s_addc_u32 s65, s63, 0
	v_mul_f32_e32 v191, v236, v237
	s_lshr_b32 s66, s41, 7
	v_pk_mul_f32 v[192:193], v[188:189], v[190:191]
	s_bfe_u32 s67, s20, 0x1000c
	v_mul_f32_e32 v162, v192, v193
	s_add_i32 s66, s66, s67
	v_rcp_f32_e32 v173, v162
	s_lshl_b32 s66, s66, 14
	v_pk_add_f32 v[164:165], v[114:115], v[116:117]
	s_lshl_b32 s67, s42, 2
	v_pk_add_f32 v[164:165], v[164:165], v[78:79]
	s_add_u32 s66, s66, s67
	v_pk_add_f32 v[164:165], v[164:165], v[80:81]
	s_add_u32 s66, s14, s66
	v_pk_add_f32 v[164:165], v[164:165], v[106:107]
	s_addc_u32 s67, s15, 0
	v_pk_add_f32 v[164:165], v[164:165], v[108:109]
	v_pk_add_f32 v[164:165], v[164:165], v[70:71]
	v_pk_add_f32 v[164:165], v[164:165], v[72:73]
	v_pk_mul_f32 v[230:231], v[172:173], v[192:193] op_sel:[1,1] op_sel_hi:[1,0]
	v_pk_mul_f32 v[192:193], v[230:231], v[190:191]
	v_pk_mul_f32 v[190:191], v[230:231], v[188:189]
	v_pk_mul_f32 v[136:137], v[192:193], v[134:135] op_sel:[0,1] op_sel_hi:[0,0]
	v_pk_mul_f32 v[148:149], v[190:191], v[146:147] op_sel:[0,1] op_sel_hi:[0,0]
	v_pk_mul_f32 v[182:183], v[192:193], v[180:181] op_sel:[1,1] op_sel_hi:[1,0]
	v_pk_mul_f32 v[238:239], v[190:191], v[236:237] op_sel:[1,1] op_sel_hi:[1,0]
	v_pk_fma_f32 v[138:139], v[136:137], v[246:247], 1.0 op_sel_hi:[1,1,0]
	v_pk_fma_f32 v[140:141], v[136:137], v[244:245], 1.0 op_sel_hi:[1,1,0]
	v_pk_fma_f32 v[150:151], v[148:149], v[250:251], 1.0 op_sel_hi:[1,1,0]
	v_pk_fma_f32 v[152:153], v[148:149], v[248:249], 1.0 op_sel_hi:[1,1,0]
	v_pk_fma_f32 v[184:185], v[182:183], v[254:255], 1.0 op_sel_hi:[1,1,0]
	v_pk_fma_f32 v[186:187], v[182:183], v[252:253], 1.0 op_sel_hi:[1,1,0]
	v_pk_fma_f32 v[240:241], v[238:239], v[234:235], 1.0 op_sel_hi:[1,1,0]
	v_pk_fma_f32 v[242:243], v[238:239], v[232:233], 1.0 op_sel_hi:[1,1,0]
	v_cvt_pk_bf16_f32 v154, v138, v139
	v_cvt_pk_bf16_f32 v155, v140, v141
	v_cvt_pk_bf16_f32 v156, v150, v151
	v_cvt_pk_bf16_f32 v157, v152, v153
	v_cvt_pk_bf16_f32 v158, v184, v185
	v_cvt_pk_bf16_f32 v159, v186, v187
	v_cvt_pk_bf16_f32 v160, v240, v241
	v_cvt_pk_bf16_f32 v161, v242, v243
	ds_read_b128 v[114:117], v172
	ds_read_b128 v[78:81], v172 offset:64
	ds_read_b128 v[106:109], v172 offset:128
	ds_read_b128 v[70:73], v172 offset:192
	v_permlane16_swap_b32_e32 v154, v156
	v_permlane16_swap_b32_e32 v155, v157
	global_store_dwordx4 v228, v[154:157], s[58:59] nt
	s_bitcmp1_b32 s20, 12
	s_cbranch_scc1 .Lg1_noX
	s_barrier
.Lg1_noX:
	v_permlane16_swap_b32_e32 v158, v160
	v_permlane16_swap_b32_e32 v159, v161
	global_store_dwordx4 v228, v[158:161], s[58:59] offset:128 nt
	v_exp_f32_e32 v130, v90
	v_exp_f32_e32 v131, v91
	v_exp_f32_e32 v132, v92
	v_exp_f32_e32 v133, v93
	v_exp_f32_e32 v142, v42
	v_exp_f32_e32 v143, v43
	v_exp_f32_e32 v144, v44
	v_exp_f32_e32 v145, v45
	v_exp_f32_e32 v176, v126
	v_exp_f32_e32 v177, v127
	v_exp_f32_e32 v178, v128
	v_exp_f32_e32 v179, v129
	v_exp_f32_e32 v232, v58
	v_exp_f32_e32 v233, v59
	v_exp_f32_e32 v234, v60
	v_exp_f32_e32 v235, v61
	v_pk_fma_f32 v[130:131], v[130:131], -0.5, -0.5 op_sel_hi:[1,0,0]
	v_pk_fma_f32 v[132:133], v[132:133], -0.5, -0.5 op_sel_hi:[1,0,0]
	v_pk_fma_f32 v[142:143], v[142:143], -0.5, -0.5 op_sel_hi:[1,0,0]
	v_pk_fma_f32 v[144:145], v[144:145], -0.5, -0.5 op_sel_hi:[1,0,0]
	v_pk_fma_f32 v[176:177], v[176:177], -0.5, -0.5 op_sel_hi:[1,0,0]
	v_pk_fma_f32 v[178:179], v[178:179], -0.5, -0.5 op_sel_hi:[1,0,0]
	v_pk_fma_f32 v[232:233], v[232:233], -0.5, -0.5 op_sel_hi:[1,0,0]
	v_pk_fma_f32 v[234:235], v[234:235], -0.5, -0.5 op_sel_hi:[1,0,0]
	v_pk_mul_f32 v[134:135], v[130:131], v[132:133]
	v_pk_mul_f32 v[146:147], v[142:143], v[144:145]
	v_pk_mul_f32 v[180:181], v[176:177], v[178:179]
	v_pk_mul_f32 v[236:237], v[232:233], v[234:235]
	v_mul_f32_e32 v188, v134, v135
	v_mul_f32_e32 v190, v146, v147
	v_mul_f32_e32 v189, v180, v181
	v_mul_f32_e32 v191, v236, v237
	v_pk_mul_f32 v[192:193], v[188:189], v[190:191]
	v_mul_f32_e32 v174, v192, v193
	v_rcp_f32_e32 v173, v174
	v_pk_add_f32 v[164:165], v[164:165], v[90:91]
	v_pk_add_f32 v[164:165], v[164:165], v[92:93]
	v_pk_add_f32 v[164:165], v[164:165], v[42:43]
	v_pk_add_f32 v[164:165], v[164:165], v[44:45]
	v_pk_add_f32 v[164:165], v[164:165], v[126:127]
	v_pk_add_f32 v[164:165], v[164:165], v[128:129]
	v_pk_add_f32 v[164:165], v[164:165], v[58:59]
	v_pk_add_f32 v[164:165], v[164:165], v[60:61]
	v_pk_mul_f32 v[230:231], v[172:173], v[192:193] op_sel:[1,1] op_sel_hi:[1,0]
	v_pk_mul_f32 v[192:193], v[230:231], v[190:191]
	v_pk_mul_f32 v[190:191], v[230:231], v[188:189]
	v_pk_mul_f32 v[136:137], v[192:193], v[134:135] op_sel:[0,1] op_sel_hi:[0,0]
	v_pk_mul_f32 v[148:149], v[190:191], v[146:147] op_sel:[0,1] op_sel_hi:[0,0]
	v_pk_mul_f32 v[182:183], v[192:193], v[180:181] op_sel:[1,1] op_sel_hi:[1,0]
	v_pk_mul_f32 v[238:239], v[190:191], v[236:237] op_sel:[1,1] op_sel_hi:[1,0]
	v_pk_fma_f32 v[138:139], v[136:137], v[132:133], 1.0 op_sel_hi:[1,1,0]
	v_pk_fma_f32 v[140:141], v[136:137], v[130:131], 1.0 op_sel_hi:[1,1,0]
	v_pk_fma_f32 v[150:151], v[148:149], v[144:145], 1.0 op_sel_hi:[1,1,0]
	v_pk_fma_f32 v[152:153], v[148:149], v[142:143], 1.0 op_sel_hi:[1,1,0]
	v_pk_fma_f32 v[184:185], v[182:183], v[178:179], 1.0 op_sel_hi:[1,1,0]
	v_pk_fma_f32 v[186:187], v[182:183], v[176:177], 1.0 op_sel_hi:[1,1,0]
	v_pk_fma_f32 v[240:241], v[238:239], v[234:235], 1.0 op_sel_hi:[1,1,0]
	v_pk_fma_f32 v[242:243], v[238:239], v[232:233], 1.0 op_sel_hi:[1,1,0]
	v_cvt_pk_bf16_f32 v154, v138, v139
	v_cvt_pk_bf16_f32 v155, v140, v141
	v_cvt_pk_bf16_f32 v156, v150, v151
	v_cvt_pk_bf16_f32 v157, v152, v153
	v_cvt_pk_bf16_f32 v158, v184, v185
	v_cvt_pk_bf16_f32 v159, v186, v187
	v_cvt_pk_bf16_f32 v160, v240, v241
	v_cvt_pk_bf16_f32 v161, v242, v243
	ds_read_b128 v[90:93], v172 offset:512
	ds_read_b128 v[42:45], v172 offset:576
	ds_read_b128 v[126:129], v172 offset:640
	ds_read_b128 v[58:61], v172 offset:704
	v_permlane16_swap_b32_e32 v154, v156
	v_permlane16_swap_b32_e32 v155, v157
	global_store_dwordx4 v228, v[154:157], s[62:63] nt
	v_permlane16_swap_b32_e32 v158, v160
	v_permlane16_swap_b32_e32 v159, v161
	global_store_dwordx4 v228, v[158:161], s[62:63] offset:128 nt
	v_log_f32_e32 v166, v162
	v_log_f32_e32 v170, v174
	v_add_f32_e32 v168, v164, v165
	v_mul_f32_e32 v168, 0xbeb17218, v168
	v_add_f32_e32 v166, v166, v170
	v_fmac_f32_e32 v168, 0x3f317218, v166
	v_mov_b32_e32 v169, v168
	s_nop 1
	v_permlane16_swap_b32_e32 v168, v169
	v_add_f32_e32 v168, v168, v169
	v_mov_b32_e32 v169, v168
	s_nop 1
	v_permlane32_swap_b32_e32 v168, v169
	v_add_f32_e32 v168, v168, v169
	s_mov_b64 exec, s[0:1]
	global_store_dword v229, v168, s[66:67]
	s_mov_b64 exec, -1
	v_exp_f32_e32 v130, v110
	v_exp_f32_e32 v131, v111
	v_exp_f32_e32 v132, v112
	v_exp_f32_e32 v133, v113
	v_exp_f32_e32 v142, v74
	v_exp_f32_e32 v143, v75
	v_exp_f32_e32 v144, v76
	v_exp_f32_e32 v145, v77
	v_exp_f32_e32 v176, v102
	v_exp_f32_e32 v177, v103
	v_exp_f32_e32 v178, v104
	v_exp_f32_e32 v179, v105
	v_exp_f32_e32 v232, v66
	v_exp_f32_e32 v233, v67
	v_exp_f32_e32 v234, v68
	v_exp_f32_e32 v235, v69
	v_pk_fma_f32 v[130:131], v[130:131], -0.5, -0.5 op_sel_hi:[1,0,0]
	v_pk_fma_f32 v[132:133], v[132:133], -0.5, -0.5 op_sel_hi:[1,0,0]
	v_pk_fma_f32 v[142:143], v[142:143], -0.5, -0.5 op_sel_hi:[1,0,0]
	v_pk_fma_f32 v[144:145], v[144:145], -0.5, -0.5 op_sel_hi:[1,0,0]
	v_pk_fma_f32 v[176:177], v[176:177], -0.5, -0.5 op_sel_hi:[1,0,0]
	v_pk_fma_f32 v[178:179], v[178:179], -0.5, -0.5 op_sel_hi:[1,0,0]
	v_pk_fma_f32 v[232:233], v[232:233], -0.5, -0.5 op_sel_hi:[1,0,0]
	v_pk_fma_f32 v[234:235], v[234:235], -0.5, -0.5 op_sel_hi:[1,0,0]
	v_pk_mul_f32 v[134:135], v[130:131], v[132:133]
	v_pk_mul_f32 v[146:147], v[142:143], v[144:145]
	v_pk_mul_f32 v[180:181], v[176:177], v[178:179]
	v_pk_mul_f32 v[236:237], v[232:233], v[234:235]
	v_mul_f32_e32 v188, v134, v135
	v_mul_f32_e32 v190, v146, v147
	v_mul_f32_e32 v189, v180, v181
	v_mul_f32_e32 v191, v236, v237
	v_pk_mul_f32 v[192:193], v[188:189], v[190:191]
	v_mul_f32_e32 v162, v192, v193
	v_rcp_f32_e32 v173, v162
	v_pk_add_f32 v[164:165], v[110:111], v[112:113]
	v_pk_add_f32 v[164:165], v[164:165], v[74:75]
	v_pk_add_f32 v[164:165], v[164:165], v[76:77]
	v_pk_add_f32 v[164:165], v[164:165], v[102:103]
	v_pk_add_f32 v[164:165], v[164:165], v[104:105]
	v_pk_add_f32 v[164:165], v[164:165], v[66:67]
	v_pk_add_f32 v[164:165], v[164:165], v[68:69]
	v_pk_mul_f32 v[230:231], v[172:173], v[192:193] op_sel:[1,1] op_sel_hi:[1,0]
	v_pk_mul_f32 v[192:193], v[230:231], v[190:191]
	v_pk_mul_f32 v[190:191], v[230:231], v[188:189]
	v_pk_mul_f32 v[136:137], v[192:193], v[134:135] op_sel:[0,1] op_sel_hi:[0,0]
	v_pk_mul_f32 v[148:149], v[190:191], v[146:147] op_sel:[0,1] op_sel_hi:[0,0]
	v_pk_mul_f32 v[182:183], v[192:193], v[180:181] op_sel:[1,1] op_sel_hi:[1,0]
	v_pk_mul_f32 v[238:239], v[190:191], v[236:237] op_sel:[1,1] op_sel_hi:[1,0]
	v_pk_fma_f32 v[138:139], v[136:137], v[132:133], 1.0 op_sel_hi:[1,1,0]
	v_pk_fma_f32 v[140:141], v[136:137], v[130:131], 1.0 op_sel_hi:[1,1,0]
	v_pk_fma_f32 v[150:151], v[148:149], v[144:145], 1.0 op_sel_hi:[1,1,0]
	v_pk_fma_f32 v[152:153], v[148:149], v[142:143], 1.0 op_sel_hi:[1,1,0]
	v_pk_fma_f32 v[184:185], v[182:183], v[178:179], 1.0 op_sel_hi:[1,1,0]
	v_pk_fma_f32 v[186:187], v[182:183], v[176:177], 1.0 op_sel_hi:[1,1,0]
	v_pk_fma_f32 v[240:241], v[238:239], v[234:235], 1.0 op_sel_hi:[1,1,0]
	v_pk_fma_f32 v[242:243], v[238:239], v[232:233], 1.0 op_sel_hi:[1,1,0]
	v_cvt_pk_bf16_f32 v154, v138, v139
	v_cvt_pk_bf16_f32 v155, v140, v141
	v_cvt_pk_bf16_f32 v156, v150, v151
	v_cvt_pk_bf16_f32 v157, v152, v153
	v_cvt_pk_bf16_f32 v158, v184, v185
	v_cvt_pk_bf16_f32 v159, v186, v187
	v_cvt_pk_bf16_f32 v160, v240, v241
	v_cvt_pk_bf16_f32 v161, v242, v243
	ds_read_b128 v[110:113], v172
	ds_read_b128 v[74:77], v172 offset:64
	ds_read_b128 v[102:105], v172 offset:128
	ds_read_b128 v[66:69], v172 offset:192
	v_permlane16_swap_b32_e32 v154, v156
	v_permlane16_swap_b32_e32 v155, v157
	global_store_dwordx4 v228, v[154:157], s[58:59] offset:2048 nt
	v_permlane16_swap_b32_e32 v158, v160
	v_permlane16_swap_b32_e32 v159, v161
	global_store_dwordx4 v228, v[158:161], s[58:59] offset:2176 nt
	v_exp_f32_e32 v130, v86
	v_exp_f32_e32 v131, v87
	v_exp_f32_e32 v132, v88
	v_exp_f32_e32 v133, v89
	v_exp_f32_e32 v142, v38
	v_exp_f32_e32 v143, v39
	v_exp_f32_e32 v144, v40
	v_exp_f32_e32 v145, v41
	v_exp_f32_e32 v176, v122
	v_exp_f32_e32 v177, v123
	v_exp_f32_e32 v178, v124
	v_exp_f32_e32 v179, v125
	v_exp_f32_e32 v232, v50
	v_exp_f32_e32 v233, v51
	v_exp_f32_e32 v234, v52
	v_exp_f32_e32 v235, v53
	v_pk_fma_f32 v[130:131], v[130:131], -0.5, -0.5 op_sel_hi:[1,0,0]
	v_pk_fma_f32 v[132:133], v[132:133], -0.5, -0.5 op_sel_hi:[1,0,0]
	v_pk_fma_f32 v[142:143], v[142:143], -0.5, -0.5 op_sel_hi:[1,0,0]
	v_pk_fma_f32 v[144:145], v[144:145], -0.5, -0.5 op_sel_hi:[1,0,0]
	v_pk_fma_f32 v[176:177], v[176:177], -0.5, -0.5 op_sel_hi:[1,0,0]
	v_pk_fma_f32 v[178:179], v[178:179], -0.5, -0.5 op_sel_hi:[1,0,0]
	v_pk_fma_f32 v[232:233], v[232:233], -0.5, -0.5 op_sel_hi:[1,0,0]
	v_pk_fma_f32 v[234:235], v[234:235], -0.5, -0.5 op_sel_hi:[1,0,0]
	v_pk_mul_f32 v[134:135], v[130:131], v[132:133]
	v_pk_mul_f32 v[146:147], v[142:143], v[144:145]
	v_pk_mul_f32 v[180:181], v[176:177], v[178:179]
	v_pk_mul_f32 v[236:237], v[232:233], v[234:235]
	v_mul_f32_e32 v188, v134, v135
	v_mul_f32_e32 v190, v146, v147
	v_mul_f32_e32 v189, v180, v181
	v_mul_f32_e32 v191, v236, v237
	v_pk_mul_f32 v[192:193], v[188:189], v[190:191]
	v_mul_f32_e32 v174, v192, v193
	v_rcp_f32_e32 v173, v174
	v_pk_add_f32 v[164:165], v[164:165], v[86:87]
	v_pk_add_f32 v[164:165], v[164:165], v[88:89]
	v_pk_add_f32 v[164:165], v[164:165], v[38:39]
	v_pk_add_f32 v[164:165], v[164:165], v[40:41]
	v_pk_add_f32 v[164:165], v[164:165], v[122:123]
	v_pk_add_f32 v[164:165], v[164:165], v[124:125]
	v_pk_add_f32 v[164:165], v[164:165], v[50:51]
	v_pk_add_f32 v[164:165], v[164:165], v[52:53]
	v_pk_mul_f32 v[230:231], v[172:173], v[192:193] op_sel:[1,1] op_sel_hi:[1,0]
	v_pk_mul_f32 v[192:193], v[230:231], v[190:191]
	v_pk_mul_f32 v[190:191], v[230:231], v[188:189]
	v_pk_mul_f32 v[136:137], v[192:193], v[134:135] op_sel:[0,1] op_sel_hi:[0,0]
	v_pk_mul_f32 v[148:149], v[190:191], v[146:147] op_sel:[0,1] op_sel_hi:[0,0]
	v_pk_mul_f32 v[182:183], v[192:193], v[180:181] op_sel:[1,1] op_sel_hi:[1,0]
	v_pk_mul_f32 v[238:239], v[190:191], v[236:237] op_sel:[1,1] op_sel_hi:[1,0]
	v_pk_fma_f32 v[138:139], v[136:137], v[132:133], 1.0 op_sel_hi:[1,1,0]
	v_pk_fma_f32 v[140:141], v[136:137], v[130:131], 1.0 op_sel_hi:[1,1,0]
	v_pk_fma_f32 v[150:151], v[148:149], v[144:145], 1.0 op_sel_hi:[1,1,0]
	v_pk_fma_f32 v[152:153], v[148:149], v[142:143], 1.0 op_sel_hi:[1,1,0]
	v_pk_fma_f32 v[184:185], v[182:183], v[178:179], 1.0 op_sel_hi:[1,1,0]
	v_pk_fma_f32 v[186:187], v[182:183], v[176:177], 1.0 op_sel_hi:[1,1,0]
	v_pk_fma_f32 v[240:241], v[238:239], v[234:235], 1.0 op_sel_hi:[1,1,0]
	v_pk_fma_f32 v[242:243], v[238:239], v[232:233], 1.0 op_sel_hi:[1,1,0]
	v_cvt_pk_bf16_f32 v154, v138, v139
	v_cvt_pk_bf16_f32 v155, v140, v141
	v_cvt_pk_bf16_f32 v156, v150, v151
	v_cvt_pk_bf16_f32 v157, v152, v153
	v_cvt_pk_bf16_f32 v158, v184, v185
	v_cvt_pk_bf16_f32 v159, v186, v187
	v_cvt_pk_bf16_f32 v160, v240, v241
	v_cvt_pk_bf16_f32 v161, v242, v243
	ds_read_b128 v[86:89], v172 offset:512
	ds_read_b128 v[38:41], v172 offset:576
	ds_read_b128 v[122:125], v172 offset:640
	ds_read_b128 v[50:53], v172 offset:704
	v_permlane16_swap_b32_e32 v154, v156
	v_permlane16_swap_b32_e32 v155, v157
	global_store_dwordx4 v228, v[154:157], s[62:63] offset:2048 nt
	v_permlane16_swap_b32_e32 v158, v160
	v_permlane16_swap_b32_e32 v159, v161
	global_store_dwordx4 v228, v[158:161], s[62:63] offset:2176 nt
	v_log_f32_e32 v166, v162
	v_log_f32_e32 v170, v174
	v_add_f32_e32 v168, v164, v165
	v_mul_f32_e32 v168, 0xbeb17218, v168
	v_add_f32_e32 v166, v166, v170
	v_fmac_f32_e32 v168, 0x3f317218, v166
	v_mov_b32_e32 v169, v168
	s_nop 1
	v_permlane16_swap_b32_e32 v168, v169
	v_add_f32_e32 v168, v168, v169
	v_mov_b32_e32 v169, v168
	s_nop 1
	v_permlane32_swap_b32_e32 v168, v169
	v_add_f32_e32 v168, v168, v169
	s_mov_b64 exec, s[0:1]
	global_store_dword v229, v168, s[66:67] offset:64
	s_mov_b64 exec, -1
	v_exp_f32_e32 v130, v98
	v_exp_f32_e32 v131, v99
	v_exp_f32_e32 v132, v100
	v_exp_f32_e32 v133, v101
	v_exp_f32_e32 v142, v62
	v_exp_f32_e32 v143, v63
	v_exp_f32_e32 v144, v64
	v_exp_f32_e32 v145, v65
	v_exp_f32_e32 v176, v94
	v_exp_f32_e32 v177, v95
	v_exp_f32_e32 v178, v96
	v_exp_f32_e32 v179, v97
	v_exp_f32_e32 v232, v54
	v_exp_f32_e32 v233, v55
	v_exp_f32_e32 v234, v56
	v_exp_f32_e32 v235, v57
	v_pk_fma_f32 v[130:131], v[130:131], -0.5, -0.5 op_sel_hi:[1,0,0]
	v_pk_fma_f32 v[132:133], v[132:133], -0.5, -0.5 op_sel_hi:[1,0,0]
	v_pk_fma_f32 v[142:143], v[142:143], -0.5, -0.5 op_sel_hi:[1,0,0]
	v_pk_fma_f32 v[144:145], v[144:145], -0.5, -0.5 op_sel_hi:[1,0,0]
	v_pk_fma_f32 v[176:177], v[176:177], -0.5, -0.5 op_sel_hi:[1,0,0]
	v_pk_fma_f32 v[178:179], v[178:179], -0.5, -0.5 op_sel_hi:[1,0,0]
	v_pk_fma_f32 v[232:233], v[232:233], -0.5, -0.5 op_sel_hi:[1,0,0]
	v_pk_fma_f32 v[234:235], v[234:235], -0.5, -0.5 op_sel_hi:[1,0,0]
	v_pk_mul_f32 v[134:135], v[130:131], v[132:133]
	v_pk_mul_f32 v[146:147], v[142:143], v[144:145]
	v_pk_mul_f32 v[180:181], v[176:177], v[178:179]
	v_pk_mul_f32 v[236:237], v[232:233], v[234:235]
	v_mul_f32_e32 v188, v134, v135
	v_mul_f32_e32 v190, v146, v147
	v_mul_f32_e32 v189, v180, v181
	v_mul_f32_e32 v191, v236, v237
	v_pk_mul_f32 v[192:193], v[188:189], v[190:191]
	v_mul_f32_e32 v162, v192, v193
	v_rcp_f32_e32 v173, v162
	v_pk_add_f32 v[164:165], v[98:99], v[100:101]
	v_pk_add_f32 v[164:165], v[164:165], v[62:63]
	v_pk_add_f32 v[164:165], v[164:165], v[64:65]
	v_pk_add_f32 v[164:165], v[164:165], v[94:95]
	v_pk_add_f32 v[164:165], v[164:165], v[96:97]
	v_pk_add_f32 v[164:165], v[164:165], v[54:55]
	v_pk_add_f32 v[164:165], v[164:165], v[56:57]
	v_pk_mul_f32 v[230:231], v[172:173], v[192:193] op_sel:[1,1] op_sel_hi:[1,0]
	v_pk_mul_f32 v[192:193], v[230:231], v[190:191]
	v_pk_mul_f32 v[190:191], v[230:231], v[188:189]
	v_pk_mul_f32 v[136:137], v[192:193], v[134:135] op_sel:[0,1] op_sel_hi:[0,0]
	v_pk_mul_f32 v[148:149], v[190:191], v[146:147] op_sel:[0,1] op_sel_hi:[0,0]
	v_pk_mul_f32 v[182:183], v[192:193], v[180:181] op_sel:[1,1] op_sel_hi:[1,0]
	v_pk_mul_f32 v[238:239], v[190:191], v[236:237] op_sel:[1,1] op_sel_hi:[1,0]
	v_pk_fma_f32 v[138:139], v[136:137], v[132:133], 1.0 op_sel_hi:[1,1,0]
	v_pk_fma_f32 v[140:141], v[136:137], v[130:131], 1.0 op_sel_hi:[1,1,0]
	v_pk_fma_f32 v[150:151], v[148:149], v[144:145], 1.0 op_sel_hi:[1,1,0]
	v_pk_fma_f32 v[152:153], v[148:149], v[142:143], 1.0 op_sel_hi:[1,1,0]
	v_pk_fma_f32 v[184:185], v[182:183], v[178:179], 1.0 op_sel_hi:[1,1,0]
	v_pk_fma_f32 v[186:187], v[182:183], v[176:177], 1.0 op_sel_hi:[1,1,0]
	v_pk_fma_f32 v[240:241], v[238:239], v[234:235], 1.0 op_sel_hi:[1,1,0]
	v_pk_fma_f32 v[242:243], v[238:239], v[232:233], 1.0 op_sel_hi:[1,1,0]
	v_cvt_pk_bf16_f32 v154, v138, v139
	v_cvt_pk_bf16_f32 v155, v140, v141
	v_cvt_pk_bf16_f32 v156, v150, v151
	v_cvt_pk_bf16_f32 v157, v152, v153
	v_cvt_pk_bf16_f32 v158, v184, v185
	v_cvt_pk_bf16_f32 v159, v186, v187
	v_cvt_pk_bf16_f32 v160, v240, v241
	v_cvt_pk_bf16_f32 v161, v242, v243
	ds_read_b128 v[98:101], v172
	ds_read_b128 v[62:65], v172 offset:64
	ds_read_b128 v[94:97], v172 offset:128
	ds_read_b128 v[54:57], v172 offset:192
	v_permlane16_swap_b32_e32 v154, v156
	v_permlane16_swap_b32_e32 v155, v157
	global_store_dwordx4 v228, v[154:157], s[60:61] nt
	v_permlane16_swap_b32_e32 v158, v160
	v_permlane16_swap_b32_e32 v159, v161
	global_store_dwordx4 v228, v[158:161], s[60:61] offset:128 nt
	v_exp_f32_e32 v130, v82
	v_exp_f32_e32 v131, v83
	v_exp_f32_e32 v132, v84
	v_exp_f32_e32 v133, v85
	v_exp_f32_e32 v142, v34
	v_exp_f32_e32 v143, v35
	v_exp_f32_e32 v144, v36
	v_exp_f32_e32 v145, v37
	v_exp_f32_e32 v176, v118
	v_exp_f32_e32 v177, v119
	v_exp_f32_e32 v178, v120
	v_exp_f32_e32 v179, v121
	v_exp_f32_e32 v232, v46
	v_exp_f32_e32 v233, v47
	v_exp_f32_e32 v234, v48
	v_exp_f32_e32 v235, v49
	v_pk_fma_f32 v[130:131], v[130:131], -0.5, -0.5 op_sel_hi:[1,0,0]
	v_pk_fma_f32 v[132:133], v[132:133], -0.5, -0.5 op_sel_hi:[1,0,0]
	v_pk_fma_f32 v[142:143], v[142:143], -0.5, -0.5 op_sel_hi:[1,0,0]
	v_pk_fma_f32 v[144:145], v[144:145], -0.5, -0.5 op_sel_hi:[1,0,0]
	v_pk_fma_f32 v[176:177], v[176:177], -0.5, -0.5 op_sel_hi:[1,0,0]
	v_pk_fma_f32 v[178:179], v[178:179], -0.5, -0.5 op_sel_hi:[1,0,0]
	v_pk_fma_f32 v[232:233], v[232:233], -0.5, -0.5 op_sel_hi:[1,0,0]
	v_pk_fma_f32 v[234:235], v[234:235], -0.5, -0.5 op_sel_hi:[1,0,0]
	v_pk_mul_f32 v[134:135], v[130:131], v[132:133]
	v_pk_mul_f32 v[146:147], v[142:143], v[144:145]
	v_pk_mul_f32 v[180:181], v[176:177], v[178:179]
	v_pk_mul_f32 v[236:237], v[232:233], v[234:235]
	v_mul_f32_e32 v188, v134, v135
	v_mul_f32_e32 v190, v146, v147
	v_mul_f32_e32 v189, v180, v181
	v_mul_f32_e32 v191, v236, v237
	v_pk_mul_f32 v[192:193], v[188:189], v[190:191]
	v_mul_f32_e32 v174, v192, v193
	v_rcp_f32_e32 v173, v174
	v_pk_add_f32 v[164:165], v[164:165], v[82:83]
	v_pk_add_f32 v[164:165], v[164:165], v[84:85]
	v_pk_add_f32 v[164:165], v[164:165], v[34:35]
	v_pk_add_f32 v[164:165], v[164:165], v[36:37]
	v_pk_add_f32 v[164:165], v[164:165], v[118:119]
	v_pk_add_f32 v[164:165], v[164:165], v[120:121]
	v_pk_add_f32 v[164:165], v[164:165], v[46:47]
	v_pk_add_f32 v[164:165], v[164:165], v[48:49]
	v_pk_mul_f32 v[230:231], v[172:173], v[192:193] op_sel:[1,1] op_sel_hi:[1,0]
	v_pk_mul_f32 v[192:193], v[230:231], v[190:191]
	v_pk_mul_f32 v[190:191], v[230:231], v[188:189]
	v_pk_mul_f32 v[136:137], v[192:193], v[134:135] op_sel:[0,1] op_sel_hi:[0,0]
	v_pk_mul_f32 v[148:149], v[190:191], v[146:147] op_sel:[0,1] op_sel_hi:[0,0]
	v_pk_mul_f32 v[182:183], v[192:193], v[180:181] op_sel:[1,1] op_sel_hi:[1,0]
	v_pk_mul_f32 v[238:239], v[190:191], v[236:237] op_sel:[1,1] op_sel_hi:[1,0]
	v_pk_fma_f32 v[138:139], v[136:137], v[132:133], 1.0 op_sel_hi:[1,1,0]
	v_pk_fma_f32 v[140:141], v[136:137], v[130:131], 1.0 op_sel_hi:[1,1,0]
	v_pk_fma_f32 v[150:151], v[148:149], v[144:145], 1.0 op_sel_hi:[1,1,0]
	v_pk_fma_f32 v[152:153], v[148:149], v[142:143], 1.0 op_sel_hi:[1,1,0]
	v_pk_fma_f32 v[184:185], v[182:183], v[178:179], 1.0 op_sel_hi:[1,1,0]
	v_pk_fma_f32 v[186:187], v[182:183], v[176:177], 1.0 op_sel_hi:[1,1,0]
	v_pk_fma_f32 v[240:241], v[238:239], v[234:235], 1.0 op_sel_hi:[1,1,0]
	v_pk_fma_f32 v[242:243], v[238:239], v[232:233], 1.0 op_sel_hi:[1,1,0]
	v_cvt_pk_bf16_f32 v154, v138, v139
	v_cvt_pk_bf16_f32 v155, v140, v141
	v_cvt_pk_bf16_f32 v156, v150, v151
	v_cvt_pk_bf16_f32 v157, v152, v153
	v_cvt_pk_bf16_f32 v158, v184, v185
	v_cvt_pk_bf16_f32 v159, v186, v187
	v_cvt_pk_bf16_f32 v160, v240, v241
	v_cvt_pk_bf16_f32 v161, v242, v243
	ds_read_b128 v[82:85], v172 offset:512
	ds_read_b128 v[34:37], v172 offset:576
	ds_read_b128 v[118:121], v172 offset:640
	ds_read_b128 v[46:49], v172 offset:704
	v_permlane16_swap_b32_e32 v154, v156
	v_permlane16_swap_b32_e32 v155, v157
	global_store_dwordx4 v228, v[154:157], s[64:65] nt
	v_permlane16_swap_b32_e32 v158, v160
	v_permlane16_swap_b32_e32 v159, v161
	global_store_dwordx4 v228, v[158:161], s[64:65] offset:128 nt
	v_log_f32_e32 v166, v162
	v_log_f32_e32 v170, v174
	v_add_f32_e32 v168, v164, v165
	v_mul_f32_e32 v168, 0xbeb17218, v168
	v_add_f32_e32 v166, v166, v170
	v_fmac_f32_e32 v168, 0x3f317218, v166
	v_mov_b32_e32 v169, v168
	s_nop 1
	v_permlane16_swap_b32_e32 v168, v169
	v_add_f32_e32 v168, v168, v169
	v_mov_b32_e32 v169, v168
	s_nop 1
	v_permlane32_swap_b32_e32 v168, v169
	v_add_f32_e32 v168, v168, v169
	s_mov_b64 exec, s[0:1]
	global_store_dword v229, v168, s[66:67] offset:512
	s_mov_b64 exec, -1
	v_exp_f32_e32 v130, v18
	v_exp_f32_e32 v131, v19
	v_exp_f32_e32 v132, v20
	v_exp_f32_e32 v133, v21
	v_exp_f32_e32 v142, v2
	v_exp_f32_e32 v143, v3
	v_exp_f32_e32 v144, v4
	v_exp_f32_e32 v145, v5
	v_exp_f32_e32 v176, v26
	v_exp_f32_e32 v177, v27
	v_exp_f32_e32 v178, v28
	v_exp_f32_e32 v179, v29
	v_exp_f32_e32 v232, v10
	v_exp_f32_e32 v233, v11
	v_exp_f32_e32 v234, v12
	v_exp_f32_e32 v235, v13
	v_pk_fma_f32 v[130:131], v[130:131], -0.5, -0.5 op_sel_hi:[1,0,0]
	v_pk_fma_f32 v[132:133], v[132:133], -0.5, -0.5 op_sel_hi:[1,0,0]
	v_pk_fma_f32 v[142:143], v[142:143], -0.5, -0.5 op_sel_hi:[1,0,0]
	v_pk_fma_f32 v[144:145], v[144:145], -0.5, -0.5 op_sel_hi:[1,0,0]
	v_pk_fma_f32 v[176:177], v[176:177], -0.5, -0.5 op_sel_hi:[1,0,0]
	v_pk_fma_f32 v[178:179], v[178:179], -0.5, -0.5 op_sel_hi:[1,0,0]
	v_pk_fma_f32 v[232:233], v[232:233], -0.5, -0.5 op_sel_hi:[1,0,0]
	v_pk_fma_f32 v[234:235], v[234:235], -0.5, -0.5 op_sel_hi:[1,0,0]
	v_pk_mul_f32 v[134:135], v[130:131], v[132:133]
	v_pk_mul_f32 v[146:147], v[142:143], v[144:145]
	v_pk_mul_f32 v[180:181], v[176:177], v[178:179]
	v_pk_mul_f32 v[236:237], v[232:233], v[234:235]
	v_mul_f32_e32 v188, v134, v135
	v_mul_f32_e32 v190, v146, v147
	v_mul_f32_e32 v189, v180, v181
	v_mul_f32_e32 v191, v236, v237
	v_pk_mul_f32 v[192:193], v[188:189], v[190:191]
	v_mul_f32_e32 v162, v192, v193
	v_rcp_f32_e32 v173, v162
	v_pk_add_f32 v[164:165], v[18:19], v[20:21]
	v_pk_add_f32 v[164:165], v[164:165], v[2:3]
	v_pk_add_f32 v[164:165], v[164:165], v[4:5]
	v_pk_add_f32 v[164:165], v[164:165], v[26:27]
	v_pk_add_f32 v[164:165], v[164:165], v[28:29]
	v_pk_add_f32 v[164:165], v[164:165], v[10:11]
	v_pk_add_f32 v[164:165], v[164:165], v[12:13]
	v_pk_mul_f32 v[230:231], v[172:173], v[192:193] op_sel:[1,1] op_sel_hi:[1,0]
	v_pk_mul_f32 v[192:193], v[230:231], v[190:191]
	v_pk_mul_f32 v[190:191], v[230:231], v[188:189]
	v_pk_mul_f32 v[136:137], v[192:193], v[134:135] op_sel:[0,1] op_sel_hi:[0,0]
	v_pk_mul_f32 v[148:149], v[190:191], v[146:147] op_sel:[0,1] op_sel_hi:[0,0]
	v_pk_mul_f32 v[182:183], v[192:193], v[180:181] op_sel:[1,1] op_sel_hi:[1,0]
	v_pk_mul_f32 v[238:239], v[190:191], v[236:237] op_sel:[1,1] op_sel_hi:[1,0]
	v_pk_fma_f32 v[138:139], v[136:137], v[132:133], 1.0 op_sel_hi:[1,1,0]
	v_pk_fma_f32 v[140:141], v[136:137], v[130:131], 1.0 op_sel_hi:[1,1,0]
	v_pk_fma_f32 v[150:151], v[148:149], v[144:145], 1.0 op_sel_hi:[1,1,0]
	v_pk_fma_f32 v[152:153], v[148:149], v[142:143], 1.0 op_sel_hi:[1,1,0]
	v_pk_fma_f32 v[184:185], v[182:183], v[178:179], 1.0 op_sel_hi:[1,1,0]
	v_pk_fma_f32 v[186:187], v[182:183], v[176:177], 1.0 op_sel_hi:[1,1,0]
	v_pk_fma_f32 v[240:241], v[238:239], v[234:235], 1.0 op_sel_hi:[1,1,0]
	v_pk_fma_f32 v[242:243], v[238:239], v[232:233], 1.0 op_sel_hi:[1,1,0]
	v_cvt_pk_bf16_f32 v154, v138, v139
	v_cvt_pk_bf16_f32 v155, v140, v141
	v_cvt_pk_bf16_f32 v156, v150, v151
	v_cvt_pk_bf16_f32 v157, v152, v153
	v_cvt_pk_bf16_f32 v158, v184, v185
	v_cvt_pk_bf16_f32 v159, v186, v187
	v_cvt_pk_bf16_f32 v160, v240, v241
	v_cvt_pk_bf16_f32 v161, v242, v243
	ds_read_b128 v[18:21], v172
	ds_read_b128 v[2:5], v172 offset:64
	ds_read_b128 v[26:29], v172 offset:128
	ds_read_b128 v[10:13], v172 offset:192
	v_permlane16_swap_b32_e32 v154, v156
	v_permlane16_swap_b32_e32 v155, v157
	global_store_dwordx4 v228, v[154:157], s[60:61] offset:2048 nt
	v_permlane16_swap_b32_e32 v158, v160
	v_permlane16_swap_b32_e32 v159, v161
	global_store_dwordx4 v228, v[158:161], s[60:61] offset:2176 nt
	v_exp_f32_e32 v130, v22
	v_exp_f32_e32 v131, v23
	v_exp_f32_e32 v132, v24
	v_exp_f32_e32 v133, v25
	v_exp_f32_e32 v142, v6
	v_exp_f32_e32 v143, v7
	v_exp_f32_e32 v144, v8
	s_mov_b32 s2, s40
	v_exp_f32_e32 v145, v9
	s_add_i32 s40, s40, 1
	v_exp_f32_e32 v176, v30
	s_mov_b32 s41, s12
	v_exp_f32_e32 v177, v31
	s_lshl_b32 s12, s40, 5
	v_exp_f32_e32 v178, v32
	s_cmp_eq_u32 s2, 7
	v_exp_f32_e32 v179, v33
	s_cselect_b64 s[2:3], -1, 0
	v_exp_f32_e32 v232, v14
	s_and_b64 s[16:17], s[2:3], exec
	v_exp_f32_e32 v233, v15
	s_cselect_b32 s12, 0xe0, s12
	v_exp_f32_e32 v234, v16
	s_add_i32 s16, s12, s18
	v_exp_f32_e32 v235, v17
	s_lshr_b32 s12, s16, 4
	v_pk_fma_f32 v[130:131], v[130:131], -0.5, -0.5 op_sel_hi:[1,0,0]
	s_and_b32 s12, s12, 0xfffff8
	v_pk_fma_f32 v[132:133], v[132:133], -0.5, -0.5 op_sel_hi:[1,0,0]
	s_lshl_b32 s16, s16, 5
	v_pk_fma_f32 v[142:143], v[142:143], -0.5, -0.5 op_sel_hi:[1,0,0]
	s_mov_b32 s42, s35
	v_pk_fma_f32 v[144:145], v[144:145], -0.5, -0.5 op_sel_hi:[1,0,0]
	s_or_b32 s12, s12, s19
	v_pk_fma_f32 v[176:177], v[176:177], -0.5, -0.5 op_sel_hi:[1,0,0]
	s_and_b32 s35, s16, 0xf00
	v_pk_fma_f32 v[178:179], v[178:179], -0.5, -0.5 op_sel_hi:[1,0,0]
	s_lshl_b32 s16, s40, 10
	v_pk_fma_f32 v[232:233], v[232:233], -0.5, -0.5 op_sel_hi:[1,0,0]
	s_lshl_b32 s12, s12, 8
	v_pk_fma_f32 v[234:235], v[234:235], -0.5, -0.5 op_sel_hi:[1,0,0]
	s_and_b32 s43, s16, 0x400
	v_pk_mul_f32 v[134:135], v[130:131], v[132:133]
	s_or_b64 s[2:3], vcc, s[2:3]
	v_pk_mul_f32 v[146:147], v[142:143], v[144:145]
	s_lshl_b32 s44, s41, 7
	v_pk_mul_f32 v[180:181], v[176:177], v[178:179]
	v_lshl_add_u64 v[202:203], s[12:13], 2, v[196:197]
	v_pk_mul_f32 v[236:237], v[232:233], v[234:235]
	s_mov_b32 s45, 0x404000
	v_mul_f32_e32 v188, v134, v135
	s_xor_b64 s[2:3], s[2:3], -1
	v_mul_f32_e32 v190, v146, v147
	v_add_u32_e32 v194, s43, v208
	v_mul_f32_e32 v189, v180, v181
	s_mov_b32 s46, 0
	v_mul_f32_e32 v191, v236, v237
	v_pk_mul_f32 v[192:193], v[188:189], v[190:191]
	v_mul_f32_e32 v174, v192, v193
	v_rcp_f32_e32 v173, v174
	v_pk_add_f32 v[164:165], v[164:165], v[22:23]
	v_pk_add_f32 v[164:165], v[164:165], v[24:25]
	v_pk_add_f32 v[164:165], v[164:165], v[6:7]
	v_pk_add_f32 v[164:165], v[164:165], v[8:9]
	v_pk_add_f32 v[164:165], v[164:165], v[30:31]
	v_pk_add_f32 v[164:165], v[164:165], v[32:33]
	v_pk_add_f32 v[164:165], v[164:165], v[14:15]
	v_pk_add_f32 v[164:165], v[164:165], v[16:17]
	v_pk_mul_f32 v[230:231], v[172:173], v[192:193] op_sel:[1,1] op_sel_hi:[1,0]
	v_pk_mul_f32 v[192:193], v[230:231], v[190:191]
	v_pk_mul_f32 v[190:191], v[230:231], v[188:189]
	v_pk_mul_f32 v[136:137], v[192:193], v[134:135] op_sel:[0,1] op_sel_hi:[0,0]
	v_pk_mul_f32 v[148:149], v[190:191], v[146:147] op_sel:[0,1] op_sel_hi:[0,0]
	v_pk_mul_f32 v[182:183], v[192:193], v[180:181] op_sel:[1,1] op_sel_hi:[1,0]
	v_pk_mul_f32 v[238:239], v[190:191], v[236:237] op_sel:[1,1] op_sel_hi:[1,0]
	v_pk_fma_f32 v[138:139], v[136:137], v[132:133], 1.0 op_sel_hi:[1,1,0]
	v_pk_fma_f32 v[140:141], v[136:137], v[130:131], 1.0 op_sel_hi:[1,1,0]
	v_pk_fma_f32 v[150:151], v[148:149], v[144:145], 1.0 op_sel_hi:[1,1,0]
	v_pk_fma_f32 v[152:153], v[148:149], v[142:143], 1.0 op_sel_hi:[1,1,0]
	v_pk_fma_f32 v[184:185], v[182:183], v[178:179], 1.0 op_sel_hi:[1,1,0]
	v_pk_fma_f32 v[186:187], v[182:183], v[176:177], 1.0 op_sel_hi:[1,1,0]
	v_pk_fma_f32 v[240:241], v[238:239], v[234:235], 1.0 op_sel_hi:[1,1,0]
	v_pk_fma_f32 v[242:243], v[238:239], v[232:233], 1.0 op_sel_hi:[1,1,0]
	v_cvt_pk_bf16_f32 v154, v138, v139
	v_cvt_pk_bf16_f32 v155, v140, v141
	v_cvt_pk_bf16_f32 v156, v150, v151
	v_cvt_pk_bf16_f32 v157, v152, v153
	v_cvt_pk_bf16_f32 v158, v184, v185
	v_cvt_pk_bf16_f32 v159, v186, v187
	v_cvt_pk_bf16_f32 v160, v240, v241
	v_cvt_pk_bf16_f32 v161, v242, v243
	ds_read_b128 v[22:25], v172 offset:512
	ds_read_b128 v[6:9], v172 offset:576
	ds_read_b128 v[30:33], v172 offset:640
	ds_read_b128 v[14:17], v172 offset:704
	v_permlane16_swap_b32_e32 v154, v156
	v_permlane16_swap_b32_e32 v155, v157
	global_store_dwordx4 v228, v[154:157], s[64:65] offset:2048 nt
	v_permlane16_swap_b32_e32 v158, v160
	v_permlane16_swap_b32_e32 v159, v161
	global_store_dwordx4 v228, v[158:161], s[64:65] offset:2176 nt
	v_log_f32_e32 v166, v162
	v_log_f32_e32 v170, v174
	v_add_f32_e32 v168, v164, v165
	v_mul_f32_e32 v168, 0xbeb17218, v168
	v_add_f32_e32 v166, v166, v170
	v_fmac_f32_e32 v168, 0x3f317218, v166
	v_mov_b32_e32 v169, v168
	s_nop 1
	v_permlane16_swap_b32_e32 v168, v169
	v_add_f32_e32 v168, v168, v169
	v_mov_b32_e32 v169, v168
	s_nop 1
	v_permlane32_swap_b32_e32 v168, v169
	v_add_f32_e32 v168, v168, v169
	s_mov_b64 exec, s[0:1]
	global_store_dword v229, v168, s[66:67] offset:576
	s_mov_b64 exec, -1
	s_cmp_eq_u32 s40, 9
	s_cbranch_scc1 .Lg1_last_tile
	s_bitcmp1_b32 s20, 12
	s_cbranch_scc0 .Lg1_noY
	s_barrier
